# N1 token loops: 64-lane sum via DPP adds and permlane16/32 swaps instead of six dependent ds_bpermute round trips (same operand pairs and order)
# baseline (speedup 1.0000x reference)
; __device__ __forceinline__ unsigned cvt_pk_bf16(float lo, float hi) { unsigned r; asm volatile("v_cvt_pk_bf16_f32 %0, %1, %2" : "=v"(r) : "v"(lo), "v"(hi)); return r; }
; __device__ __forceinline__ unsigned pk4_fp8c(float a, float b, float c, float d) { return pk4_fp8(__builtin_amdgcn_fmed3f(a, -448.f, 448.f), __builtin_amdgcn_fmed3f(b, -448.f, 448.f), __builtin_amdgcn_fmed3f(c, -448.f, 448.f), __builtin_amdgcn_fmed3f(d, -448.f, 448.f)); }
; __device__ __forceinline__ void n1_phase(const Args& a, int layer, bool final_only, const int wv, const bool dry = false) {
;     ...
;             if (layer == 0) ld_row16(a.x + (size_t)tok * DM, F.lane, v);
;     ...
;             if (final_only) continue;
;             float ss = 0.f;
; #pragma unroll
;             for (int j = 0; j < 4; ++j) ss += v[j][0] * v[j][0] + v[j][1] * v[j][1] + v[j][2] * v[j][2] + v[j][3] * v[j][3];
;             const float inv = rsqrtf(wave_sum(ss, F.lane) * (1.f / DM) + EPS);
; #pragma unroll
;             for (int j = 0; j < 4; ++j) { const int c0 = 4 * F.lane + 256 * j;
;                 const f32x4 h = v[j] * inv * ma[j] + mb[j];
;                 if (layer & 1) *(unsigned*)((unsigned char*)HM + (size_t)tok * DM + c0) = pg8::pk4_fp8c(h[0] * FP8_HSC, h[1] * FP8_HSC, h[2] * FP8_HSC, h[3] * FP8_HSC);
;                 else { u32x2 o; o.x = cvt_pk_bf16(h[0], h[1]); o.y = cvt_pk_bf16(h[2], h[3]); *(u32x2*)(HM + (size_t)tok * DM + c0) = o; } }
.LBB0_165:
	global_load_dwordx4 v[54:57], v[24:25], off offset:-2048
	global_load_dwordx4 v[58:61], v[24:25], off offset:-1024
	global_load_dwordx4 v[62:65], v[24:25], off
	global_load_dwordx4 v[66:69], v[24:25], off offset:1024
	v_lshl_add_u64 v[70:71], v[22:23], 0, s[6:7]
	v_add_co_u32_e32 v70, vcc, s15, v70
	s_add_u32 s6, s6, 0x800
	s_nop 0
	v_addc_co_u32_e32 v71, vcc, 0, v71, vcc
	s_addc_u32 s7, s7, 0
	v_lshl_add_u64 v[24:25], v[24:25], 0, s[4:5]
	s_cmpk_eq_u32 s6, 0x8000
	s_waitcnt vmcnt(3)
	v_mov_b32_e32 v74, v55
	s_waitcnt vmcnt(2)
	v_mov_b32_e32 v75, v59
	v_mov_b32_e32 v72, v54
	v_mov_b32_e32 v73, v58
	s_waitcnt vmcnt(1)
	v_mov_b32_e32 v78, v63
	s_waitcnt vmcnt(0)
	v_mov_b32_e32 v79, v67
	v_pk_mul_f32 v[74:75], v[74:75], v[74:75]
	v_mov_b32_e32 v76, v62
	v_mov_b32_e32 v77, v66
	v_mov_b32_e32 v80, v56
	v_mov_b32_e32 v81, v60
	v_pk_mul_f32 v[78:79], v[78:79], v[78:79]
	v_pk_fma_f32 v[72:73], v[72:73], v[72:73], v[74:75]
	v_mov_b32_e32 v82, v64
	v_mov_b32_e32 v83, v68
	v_mov_b32_e32 v84, v57
	v_mov_b32_e32 v85, v61
	v_pk_fma_f32 v[74:75], v[76:77], v[76:77], v[78:79]
	v_pk_fma_f32 v[72:73], v[80:81], v[80:81], v[72:73]
	v_mov_b32_e32 v86, v65
	v_mov_b32_e32 v87, v69
	v_pk_fma_f32 v[74:75], v[82:83], v[82:83], v[74:75]
	v_pk_fma_f32 v[72:73], v[84:85], v[84:85], v[72:73]
	v_pk_fma_f32 v[74:75], v[86:87], v[86:87], v[74:75]
	v_add_f32_e32 v53, v72, v73
	v_add_f32_e32 v53, v53, v74
	v_add_f32_e32 v53, v53, v75
	s_waitcnt lgkmcnt(0)
	s_nop 1
	v_add_f32_dpp v53, v53, v53 quad_perm:[1,0,3,2] row_mask:0xf bank_mask:0xf
	s_nop 1
	v_add_f32_dpp v53, v53, v53 quad_perm:[2,3,0,1] row_mask:0xf bank_mask:0xf
	s_nop 1
	v_add_f32_dpp v53, v53, v53 row_half_mirror row_mask:0xf bank_mask:0xf
	s_nop 1
	v_add_f32_dpp v53, v53, v53 row_mirror row_mask:0xf bank_mask:0xf
	v_mov_b32_e32 v72, v53
	s_nop 1
	v_permlane16_swap_b32_e32 v53, v72
	v_add_f32_e32 v53, v53, v72
	v_mov_b32_e32 v72, v53
	s_nop 1
	v_permlane32_swap_b32_e32 v53, v72
	v_add_f32_e32 v53, v53, v72
	v_fmamk_f32 v53, v53, 0x3a800000, v52
	v_mul_f32_e32 v72, 0x4b800000, v53
	v_cmp_gt_f32_e32 vcc, s14, v53
	s_nop 1
	v_cndmask_b32_e32 v53, v53, v72, vcc
	v_rsq_f32_e32 v53, v53
	s_nop 0
	v_mul_f32_e32 v72, 0x45800000, v53
	v_cndmask_b32_e32 v72, v53, v72, vcc
	v_pk_mul_f32 v[54:55], v[54:55], v[72:73] op_sel_hi:[1,0]
	v_pk_mul_f32 v[56:57], v[56:57], v[72:73] op_sel_hi:[1,0]
	v_pk_fma_f32 v[54:55], v[28:29], v[54:55], v[0:1]
	v_pk_mul_f32 v[58:59], v[58:59], v[72:73] op_sel_hi:[1,0]
	v_pk_mul_f32 v[60:61], v[60:61], v[72:73] op_sel_hi:[1,0]
	v_pk_fma_f32 v[56:57], v[26:27], v[56:57], v[2:3]
	v_cvt_pk_bf16_f32 v54, v54, v55
	v_pk_mul_f32 v[62:63], v[62:63], v[72:73] op_sel_hi:[1,0]
	v_cvt_pk_bf16_f32 v55, v56, v57
	v_pk_mul_f32 v[64:65], v[64:65], v[72:73] op_sel_hi:[1,0]
	v_pk_fma_f32 v[60:61], v[30:31], v[60:61], v[6:7]
	v_pk_fma_f32 v[58:59], v[32:33], v[58:59], v[4:5]
	global_store_dwordx2 v[70:71], v[54:55], off
	v_cvt_pk_bf16_f32 v54, v58, v59
	v_cvt_pk_bf16_f32 v55, v60, v61
	v_pk_mul_f32 v[66:67], v[66:67], v[72:73] op_sel_hi:[1,0]
	v_pk_mul_f32 v[68:69], v[68:69], v[72:73] op_sel_hi:[1,0]
	v_pk_fma_f32 v[64:65], v[34:35], v[64:65], v[10:11]
	v_pk_fma_f32 v[62:63], v[36:37], v[62:63], v[8:9]
	global_store_dwordx2 v[70:71], v[54:55], off offset:512
	v_cvt_pk_bf16_f32 v54, v62, v63
	v_cvt_pk_bf16_f32 v55, v64, v65
	v_pk_fma_f32 v[68:69], v[38:39], v[68:69], v[14:15]
	v_pk_fma_f32 v[66:67], v[40:41], v[66:67], v[12:13]
	global_store_dwordx2 v[70:71], v[54:55], off offset:1024
	v_cvt_pk_bf16_f32 v54, v66, v67
	v_cvt_pk_bf16_f32 v55, v68, v69
	global_store_dwordx2 v[70:71], v[54:55], off offset:1536
	s_cbranch_scc0 .LBB0_165
	s_add_i32 s9, s9, s12
	s_add_i32 s2, s2, s13
	s_cmpk_gt_i32 s9, 0x7ff
	s_cbranch_scc0 .LBB0_164

; __device__ __forceinline__ void n1_phase(const Args& a, int layer, bool final_only, const int wv, const bool dry = false) {
;     ...
; #pragma unroll 1
;         for (int i = 0; i < 16; ++i) {
;             const int tok = tok0 + i;
;             f32x4 v[4];
;             if (layer == 0) ld_row16(a.x + (size_t)tok * DM, F.lane, v);
;             else {
; #pragma unroll
;                 for (int j = 0; j < 4; ++j) { const u32x2 w = *(const u32x2*)(XB + (size_t)tok * DM + 4 * F.lane + 256 * j); v[j] = (f32x4){bf_lo(w.x), bf_hi(w.x), bf_lo(w.y), bf_hi(w.y)}; } }
;             if (combine) {
;                 f32x4 ysum[4];
; #pragma unroll
;                 for (int j = 0; j < 4; ++j) ysum[j] = (f32x4){0.f, 0.f, 0.f, 0.f};
; #pragma unroll
;                 for (int k = 0; k < 4; ++k) { const int e = toke[tok * 4 + k], r = tokr[tok * 4 + k]; const size_t slot = (size_t)ps[e] + r;
;                     const unsigned char* yr = Y + slot * DM + 4 * F.lane;
; #pragma unroll
;                     for (int j = 0; j < 4; ++j) { const int w = *(const int*)(yr + 256 * j); const f32x2 lo = __builtin_amdgcn_cvt_pk_f32_fp8(w, false), hi = __builtin_amdgcn_cvt_pk_f32_fp8(w, true);
;                         ysum[j][0] += lo[0]; ysum[j][1] += lo[1]; ysum[j][2] += hi[0]; ysum[j][3] += hi[1]; } }
.LBB0_1602:
	v_lshl_add_u64 v[70:71], s[4:5], 0, v[32:33]
	s_add_i32 s16, s33, s7
	v_add_co_u32_e64 v70, s[2:3], s42, v70
	s_ashr_i32 s17, s16, 31
	s_nop 0
	v_addc_co_u32_e64 v71, s[2:3], 0, v71, s[2:3]
	v_lshl_add_u64 v[68:69], s[4:5], 0, v[34:35]
	s_lshl_b64 s[2:3], s[16:17], 2
	v_add_co_u32_e32 v68, vcc, 0xaf200000, v68
	s_add_u32 s44, s23, s2
	s_nop 0
	v_addc_co_u32_e32 v69, vcc, 0, v69, vcc
	s_addc_u32 s45, s24, s3
	global_load_dwordx2 v[90:91], v[68:69], off
	global_load_dwordx2 v[92:93], v[68:69], off offset:512
	global_load_dwordx2 v[94:95], v[68:69], off offset:1024
	global_load_dwordx2 v[96:97], v[68:69], off offset:1536
	global_load_dwordx4 v[82:85], v17, s[44:45]
	s_add_u32 s2, s25, s2
	s_addc_u32 s3, s26, s3
	s_add_i32 s16, s16, 1
	s_ashr_i32 s17, s16, 31
	global_load_dword v98, v17, s[2:3]
	s_lshl_b64 s[2:3], s[16:17], 2
	s_add_u32 s2, s25, s2
	s_addc_u32 s3, s26, s3
	global_load_dwordx3 v[86:88], v17, s[2:3]
	v_mov_b32_e32 v162, 0
	v_mov_b32_e32 v163, 0
	v_mov_b32_e32 v164, 0
	v_mov_b32_e32 v165, 0
	s_add_i32 s7, s7, 4
	v_lshl_add_u64 v[32:33], v[32:33], 0, s[12:13]
	v_lshl_add_u64 v[34:35], v[34:35], 0, s[14:15]
	s_cmp_eq_u32 s7, 64
	s_waitcnt vmcnt(6)
	v_lshlrev_b32_e32 v100, 16, v90
	v_and_b32_e32 v101, 0xffff0000, v90
	s_waitcnt vmcnt(5)
	v_lshlrev_b32_e32 v102, 16, v92
	v_and_b32_e32 v103, 0xffff0000, v92
	s_waitcnt vmcnt(2)
	v_lshlrev_b32_e32 v82, 2, v82
	v_lshlrev_b32_e32 v83, 2, v83
	v_lshlrev_b32_e32 v84, 2, v84
	v_lshlrev_b32_e32 v85, 2, v85
	v_add_u32_e32 v82, s39, v82
	v_add_u32_e32 v83, s39, v83
	v_add_u32_e32 v89, s39, v84
	v_add_u32_e32 v85, s39, v85
	ds_read_b32 v82, v82
	ds_read_b32 v84, v83
	ds_read_b32 v108, v89
	ds_read_b32 v110, v85
	s_waitcnt vmcnt(1)
	v_ashrrev_i32_e32 v99, 31, v98
	s_waitcnt lgkmcnt(3)
	v_ashrrev_i32_e32 v83, 31, v82
	s_waitcnt vmcnt(0)
	v_ashrrev_i32_e32 v113, 31, v86
	v_mov_b32_e32 v112, v86
	v_ashrrev_i32_e32 v115, 31, v87
	v_mov_b32_e32 v114, v87
	v_ashrrev_i32_e32 v87, 31, v88
	v_mov_b32_e32 v86, v88
	s_waitcnt lgkmcnt(2)
	v_ashrrev_i32_e32 v85, 31, v84
	s_waitcnt lgkmcnt(1)
	v_ashrrev_i32_e32 v109, 31, v108
	s_waitcnt lgkmcnt(0)
	v_ashrrev_i32_e32 v111, 31, v110
	v_lshl_add_u64 v[82:83], v[82:83], 0, v[98:99]
	v_lshl_add_u64 v[84:85], v[84:85], 0, v[112:113]
	v_lshl_add_u64 v[88:89], v[108:109], 0, v[114:115]
	v_lshl_add_u64 v[86:87], v[110:111], 0, v[86:87]
	v_lshlrev_b64 v[82:83], 10, v[82:83]
	v_lshlrev_b64 v[84:85], 10, v[84:85]
	v_lshlrev_b64 v[88:89], 10, v[88:89]
	v_lshlrev_b64 v[86:87], 10, v[86:87]
	v_lshl_add_u64 v[82:83], v[18:19], 0, v[82:83]
	v_lshl_add_u64 v[84:85], v[18:19], 0, v[84:85]
	v_lshl_add_u64 v[88:89], v[18:19], 0, v[88:89]
	v_lshl_add_u64 v[86:87], v[18:19], 0, v[86:87]
	global_load_dword v98, v[82:83], off
	global_load_dword v99, v[82:83], off offset:256
	global_load_dword v108, v[82:83], off offset:512
	global_load_dword v112, v[82:83], off offset:768
	global_load_dword v116, v[84:85], off
	global_load_dword v120, v[84:85], off offset:256
	global_load_dword v124, v[84:85], off offset:512
	global_load_dword v128, v[84:85], off offset:768
	global_load_dword v132, v[88:89], off
	global_load_dword v136, v[88:89], off offset:256
	global_load_dword v140, v[88:89], off offset:512
	global_load_dword v144, v[88:89], off offset:768
	global_load_dword v148, v[86:87], off
	global_load_dword v152, v[86:87], off offset:256
	global_load_dword v156, v[86:87], off offset:512
	global_load_dword v160, v[86:87], off offset:768
	v_lshlrev_b32_e32 v90, 16, v91
	v_and_b32_e32 v91, 0xffff0000, v91
	v_lshlrev_b32_e32 v92, 16, v93
	v_and_b32_e32 v93, 0xffff0000, v93
	v_lshlrev_b32_e32 v104, 16, v94
	v_and_b32_e32 v105, 0xffff0000, v94
	v_lshlrev_b32_e32 v94, 16, v95
	v_and_b32_e32 v95, 0xffff0000, v95
	v_lshlrev_b32_e32 v106, 16, v96
	v_and_b32_e32 v107, 0xffff0000, v96
	v_lshlrev_b32_e32 v96, 16, v97
	v_and_b32_e32 v97, 0xffff0000, v97
	s_waitcnt vmcnt(15)
	v_cvt_pk_f32_fp8_e32 v[82:83], v98
	s_waitcnt vmcnt(14)
	v_cvt_pk_f32_fp8_e32 v[86:87], v99
	v_cvt_pk_f32_fp8_sdwa v[84:85], v98 src0_sel:WORD_1
	v_cvt_pk_f32_fp8_sdwa v[88:89], v99 src0_sel:WORD_1
	s_waitcnt vmcnt(13)
	v_cvt_pk_f32_fp8_e32 v[98:99], v108
	v_cvt_pk_f32_fp8_sdwa v[108:109], v108 src0_sel:WORD_1
	s_waitcnt vmcnt(12)
	v_cvt_pk_f32_fp8_e32 v[110:111], v112
	v_cvt_pk_f32_fp8_sdwa v[112:113], v112 src0_sel:WORD_1
	s_waitcnt vmcnt(11)
	v_cvt_pk_f32_fp8_e32 v[114:115], v116
	s_waitcnt vmcnt(10)
	v_cvt_pk_f32_fp8_e32 v[118:119], v120
	v_cvt_pk_f32_fp8_sdwa v[116:117], v116 src0_sel:WORD_1
	v_cvt_pk_f32_fp8_sdwa v[120:121], v120 src0_sel:WORD_1
	s_waitcnt vmcnt(9)
	v_cvt_pk_f32_fp8_e32 v[122:123], v124
	v_cvt_pk_f32_fp8_sdwa v[124:125], v124 src0_sel:WORD_1
	s_waitcnt vmcnt(8)
	v_cvt_pk_f32_fp8_e32 v[126:127], v128
	v_cvt_pk_f32_fp8_sdwa v[128:129], v128 src0_sel:WORD_1
	s_waitcnt vmcnt(7)
	v_cvt_pk_f32_fp8_e32 v[130:131], v132
	s_waitcnt vmcnt(6)
	v_cvt_pk_f32_fp8_e32 v[134:135], v136
	v_cvt_pk_f32_fp8_sdwa v[132:133], v132 src0_sel:WORD_1
	v_cvt_pk_f32_fp8_sdwa v[136:137], v136 src0_sel:WORD_1
	s_waitcnt vmcnt(5)
	v_cvt_pk_f32_fp8_e32 v[138:139], v140
	v_cvt_pk_f32_fp8_sdwa v[140:141], v140 src0_sel:WORD_1
	s_waitcnt vmcnt(4)
	v_cvt_pk_f32_fp8_e32 v[142:143], v144
	v_cvt_pk_f32_fp8_sdwa v[144:145], v144 src0_sel:WORD_1
	s_waitcnt vmcnt(3)
	v_cvt_pk_f32_fp8_e32 v[146:147], v148
	s_waitcnt vmcnt(2)
	v_cvt_pk_f32_fp8_e32 v[150:151], v152
	v_cvt_pk_f32_fp8_sdwa v[148:149], v148 src0_sel:WORD_1
	v_cvt_pk_f32_fp8_sdwa v[152:153], v152 src0_sel:WORD_1
	s_waitcnt vmcnt(1)
	v_cvt_pk_f32_fp8_e32 v[154:155], v156
	v_cvt_pk_f32_fp8_sdwa v[156:157], v156 src0_sel:WORD_1
	s_waitcnt vmcnt(0)
; __device__ __forceinline__ unsigned cvt_pk_bf16(float lo, float hi) { unsigned r; asm volatile("v_cvt_pk_bf16_f32 %0, %1, %2" : "=v"(r) : "v"(lo), "v"(hi)); return r; }
; __device__ __forceinline__ float shx(float v, int m, int lane) { return __builtin_bit_cast(float, __builtin_amdgcn_ds_bpermute((lane ^ m) << 2, __builtin_bit_cast(int, v))); }
; __device__ __forceinline__ unsigned pk4_fp8c(float a, float b, float c, float d) { return pk4_fp8(__builtin_amdgcn_fmed3f(a, -448.f, 448.f), __builtin_amdgcn_fmed3f(b, -448.f, 448.f), __builtin_amdgcn_fmed3f(c, -448.f, 448.f), __builtin_amdgcn_fmed3f(d, -448.f, 448.f)); }
; __device__ __forceinline__ float wave_sum(float v, int lane) {
; #pragma unroll
;     for (int o = 1; o < 64; o <<= 1) v += shx(v, o, lane);
;     return v;
; __device__ __forceinline__ void n1_phase(const Args& a, int layer, bool final_only, const int wv, const bool dry = false) {
;     ...
; #pragma unroll
;                 for (int j = 0; j < 4; ++j) { v[j] = v[j] + g2s[j] * ysum[j];
;                     if (final_only) *(f32x4*)(a.out + (size_t)tok * DM + 4 * F.lane + 256 * j) = v[j];
;                     else { u32x2 o; o.x = cvt_pk_bf16(v[j][0], v[j][1]); o.y = cvt_pk_bf16(v[j][2], v[j][3]); *(u32x2*)((dry ? (bf16_t*)(ws + WS_ACT) : XB) + (size_t)tok * DM + 4 * F.lane + 256 * j) = o; } }
;             }
;             if (final_only) continue;
;             float ss = 0.f;
; #pragma unroll
;             for (int j = 0; j < 4; ++j) ss += v[j][0] * v[j][0] + v[j][1] * v[j][1] + v[j][2] * v[j][2] + v[j][3] * v[j][3];
;             const float inv = rsqrtf(wave_sum(ss, F.lane) * (1.f / DM) + EPS);
; #pragma unroll
;             for (int j = 0; j < 4; ++j) { const int c0 = 4 * F.lane + 256 * j;
;                 const f32x4 h = v[j] * inv * ma[j] + mb[j];
;                 if (layer & 1) *(unsigned*)((unsigned char*)HM + (size_t)tok * DM + c0) = pg8::pk4_fp8c(h[0] * FP8_HSC, h[1] * FP8_HSC, h[2] * FP8_HSC, h[3] * FP8_HSC);
;                 else { u32x2 o; o.x = cvt_pk_bf16(h[0], h[1]); o.y = cvt_pk_bf16(h[2], h[3]); *(u32x2*)(HM + (size_t)tok * DM + c0) = o; } }
	v_cvt_pk_f32_fp8_e32 v[158:159], v160
	v_cvt_pk_f32_fp8_sdwa v[160:161], v160 src0_sel:WORD_1
	v_pk_add_f32 v[82:83], v[82:83], 0 op_sel_hi:[1,0]
	v_pk_add_f32 v[86:87], v[86:87], 0 op_sel_hi:[1,0]
	v_pk_add_f32 v[84:85], v[84:85], 0 op_sel_hi:[1,0]
	v_pk_add_f32 v[88:89], v[88:89], 0 op_sel_hi:[1,0]
	v_pk_add_f32 v[108:109], v[108:109], 0 op_sel_hi:[1,0]
	v_pk_add_f32 v[98:99], v[98:99], 0 op_sel_hi:[1,0]
	v_pk_add_f32 v[112:113], v[112:113], 0 op_sel_hi:[1,0]
	v_pk_add_f32 v[110:111], v[110:111], 0 op_sel_hi:[1,0]
	v_pk_add_f32 v[82:83], v[82:83], v[114:115]
	v_pk_add_f32 v[86:87], v[86:87], v[118:119]
	v_pk_add_f32 v[84:85], v[84:85], v[116:117]
	v_pk_add_f32 v[88:89], v[88:89], v[120:121]
	v_pk_add_f32 v[98:99], v[98:99], v[122:123]
	v_pk_add_f32 v[108:109], v[108:109], v[124:125]
	v_pk_add_f32 v[110:111], v[110:111], v[126:127]
	v_pk_add_f32 v[112:113], v[112:113], v[128:129]
	v_pk_add_f32 v[82:83], v[82:83], v[130:131]
	v_pk_add_f32 v[86:87], v[86:87], v[134:135]
	v_pk_add_f32 v[84:85], v[84:85], v[132:133]
	v_pk_add_f32 v[88:89], v[88:89], v[136:137]
	v_pk_add_f32 v[108:109], v[108:109], v[140:141]
	v_pk_add_f32 v[98:99], v[98:99], v[138:139]
	v_pk_add_f32 v[112:113], v[112:113], v[144:145]
	v_pk_add_f32 v[110:111], v[110:111], v[142:143]
	v_pk_add_f32 v[82:83], v[82:83], v[146:147]
	v_pk_add_f32 v[86:87], v[86:87], v[150:151]
	v_pk_add_f32 v[84:85], v[84:85], v[148:149]
	v_pk_add_f32 v[88:89], v[88:89], v[152:153]
	v_pk_add_f32 v[98:99], v[98:99], v[154:155]
	v_pk_add_f32 v[108:109], v[108:109], v[156:157]
	v_pk_add_f32 v[110:111], v[110:111], v[158:159]
	v_pk_add_f32 v[112:113], v[112:113], v[160:161]
	v_pk_fma_f32 v[82:83], v[38:39], v[82:83], v[100:101]
	v_pk_fma_f32 v[86:87], v[42:43], v[86:87], v[102:103]
	v_pk_fma_f32 v[84:85], v[36:37], v[84:85], v[90:91]
	v_pk_fma_f32 v[88:89], v[40:41], v[88:89], v[92:93]
	v_pk_fma_f32 v[90:91], v[44:45], v[108:109], v[94:95]
	v_pk_fma_f32 v[92:93], v[46:47], v[98:99], v[104:105]
	v_pk_fma_f32 v[94:95], v[48:49], v[112:113], v[96:97]
	v_pk_fma_f32 v[96:97], v[50:51], v[110:111], v[106:107]
	v_mov_b32_e32 v102, v83
	v_mov_b32_e32 v103, v87
	v_cvt_pk_bf16_f32 v98, v82, v83
	v_cvt_pk_bf16_f32 v99, v84, v85
	v_mov_b32_e32 v100, v82
	v_mov_b32_e32 v101, v86
	v_mov_b32_e32 v110, v93
	v_mov_b32_e32 v111, v97
	v_pk_mul_f32 v[102:103], v[102:103], v[102:103]
	v_mov_b32_e32 v104, v84
	v_mov_b32_e32 v105, v88
	v_mov_b32_e32 v108, v92
	v_mov_b32_e32 v109, v96
	global_store_dwordx2 v[68:69], v[98:99], off
	v_cvt_pk_bf16_f32 v98, v86, v87
	v_cvt_pk_bf16_f32 v99, v88, v89
	v_pk_mul_f32 v[110:111], v[110:111], v[110:111]
	v_pk_fma_f32 v[100:101], v[100:101], v[100:101], v[102:103]
	v_mov_b32_e32 v106, v85
	v_mov_b32_e32 v107, v89
	v_mov_b32_e32 v112, v90
	v_mov_b32_e32 v113, v94
	global_store_dwordx2 v[68:69], v[98:99], off offset:512
	v_cvt_pk_bf16_f32 v98, v92, v93
	v_cvt_pk_bf16_f32 v99, v90, v91
	v_pk_fma_f32 v[102:103], v[108:109], v[108:109], v[110:111]
	v_pk_fma_f32 v[100:101], v[104:105], v[104:105], v[100:101]
	v_mov_b32_e32 v114, v91
	v_mov_b32_e32 v115, v95
	global_store_dwordx2 v[68:69], v[98:99], off offset:1024
	v_cvt_pk_bf16_f32 v98, v96, v97
	v_cvt_pk_bf16_f32 v99, v94, v95
	v_pk_fma_f32 v[102:103], v[112:113], v[112:113], v[102:103]
	global_store_dwordx2 v[68:69], v[98:99], off offset:1536
	v_pk_fma_f32 v[68:69], v[106:107], v[106:107], v[100:101]
	v_pk_fma_f32 v[98:99], v[114:115], v[114:115], v[102:103]
	v_add_f32_e32 v68, v68, v69
	v_add_f32_e32 v68, v68, v98
	v_add_f32_e32 v68, v68, v99
	s_waitcnt lgkmcnt(0)
	s_nop 1
	v_add_f32_dpp v68, v68, v68 quad_perm:[1,0,3,2] row_mask:0xf bank_mask:0xf
	s_nop 1
	v_add_f32_dpp v68, v68, v68 quad_perm:[2,3,0,1] row_mask:0xf bank_mask:0xf
	s_nop 1
	v_add_f32_dpp v68, v68, v68 row_half_mirror row_mask:0xf bank_mask:0xf
	s_nop 1
	v_add_f32_dpp v68, v68, v68 row_mirror row_mask:0xf bank_mask:0xf
	v_mov_b32_e32 v69, v68
	s_nop 1
	v_permlane16_swap_b32_e32 v68, v69
	v_add_f32_e32 v68, v68, v69
	v_mov_b32_e32 v69, v68
	s_nop 1
	v_permlane32_swap_b32_e32 v68, v69
	v_add_f32_e32 v68, v68, v69
	v_fmamk_f32 v68, v68, 0x3a800000, v80
	v_mul_f32_e32 v69, 0x4b800000, v68
	v_cmp_gt_f32_e32 vcc, s40, v68
	s_nop 1
	v_cndmask_b32_e32 v68, v68, v69, vcc
	v_rsq_f32_e32 v68, v68
	s_nop 0
	v_mul_f32_e32 v69, 0x45800000, v68
	v_cndmask_b32_e32 v68, v68, v69, vcc
	v_pk_mul_f32 v[82:83], v[82:83], v[68:69] op_sel_hi:[1,0]
	v_pk_mul_f32 v[86:87], v[86:87], v[68:69] op_sel_hi:[1,0]
	v_pk_fma_f32 v[82:83], v[54:55], v[82:83], v[0:1]
	v_pk_mul_f32 v[92:93], v[92:93], v[68:69] op_sel_hi:[1,0]
	v_pk_fma_f32 v[86:87], v[58:59], v[86:87], v[4:5]
	v_mul_f32_e32 v82, 0x41800000, v82
	v_mul_f32_e32 v83, 0x41800000, v83
	v_pk_mul_f32 v[96:97], v[96:97], v[68:69] op_sel_hi:[1,0]
	v_pk_fma_f32 v[92:93], v[62:63], v[92:93], v[8:9]
	v_mul_f32_e32 v86, 0x41800000, v86
	v_mul_f32_e32 v87, 0x41800000, v87
	v_med3_f32 v82, v82, s41, v81
	v_med3_f32 v83, v83, s41, v81
	v_pk_mul_f32 v[84:85], v[84:85], v[68:69] op_sel_hi:[1,0]
	v_pk_mul_f32 v[88:89], v[88:89], v[68:69] op_sel_hi:[1,0]
	v_pk_mul_f32 v[90:91], v[90:91], v[68:69] op_sel_hi:[1,0]
	v_pk_mul_f32 v[68:69], v[94:95], v[68:69] op_sel_hi:[1,0]
	v_pk_fma_f32 v[94:95], v[66:67], v[96:97], v[12:13]
	v_mul_f32_e32 v92, 0x41800000, v92
	v_mul_f32_e32 v93, 0x41800000, v93
	v_med3_f32 v86, v86, s41, v81
	v_med3_f32 v87, v87, s41, v81
	v_cvt_pk_fp8_f32 v162, v82, v83
	v_pk_fma_f32 v[84:85], v[52:53], v[84:85], v[2:3]
	v_mul_f32_e32 v94, 0x41800000, v94
	v_mul_f32_e32 v95, 0x41800000, v95
	v_med3_f32 v92, v92, s41, v81
	v_med3_f32 v93, v93, s41, v81
	v_cvt_pk_fp8_f32 v163, v86, v87
	v_pk_fma_f32 v[88:89], v[56:57], v[88:89], v[6:7]
	v_mul_f32_e32 v84, 0x41800000, v84
	v_mul_f32_e32 v85, 0x41800000, v85
	v_med3_f32 v94, v94, s41, v81
	v_med3_f32 v95, v95, s41, v81
	v_cvt_pk_fp8_f32 v164, v92, v93
	v_pk_fma_f32 v[90:91], v[60:61], v[90:91], v[10:11]
	v_mul_f32_e32 v88, 0x41800000, v88
	v_mul_f32_e32 v89, 0x41800000, v89
	v_med3_f32 v84, v84, s41, v81
	v_med3_f32 v85, v85, s41, v81
	v_cvt_pk_fp8_f32 v165, v94, v95
	v_pk_fma_f32 v[68:69], v[64:65], v[68:69], v[14:15]
	v_mul_f32_e32 v90, 0x41800000, v90
	v_mul_f32_e32 v91, 0x41800000, v91
	v_med3_f32 v88, v88, s41, v81
	v_med3_f32 v89, v89, s41, v81
	v_cvt_pk_fp8_f32 v162, v84, v85 op_sel:[0,0,1]
	v_mul_f32_e32 v68, 0x41800000, v68
	v_mul_f32_e32 v69, 0x41800000, v69
	v_med3_f32 v90, v90, s41, v81
	v_med3_f32 v91, v91, s41, v81
	v_cvt_pk_fp8_f32 v163, v88, v89 op_sel:[0,0,1]
	v_med3_f32 v68, v68, s41, v81
	v_med3_f32 v69, v69, s41, v81
	v_cvt_pk_fp8_f32 v164, v90, v91 op_sel:[0,0,1]
	v_cvt_pk_fp8_f32 v165, v68, v69 op_sel:[0,0,1]
	global_store_dword v[70:71], v162, off
	global_store_dword v[70:71], v163, off offset:256
	global_store_dword v[70:71], v164, off offset:512
	global_store_dword v[70:71], v165, off offset:768
	s_cbranch_scc0 .LBB0_1602
	s_add_i32 s20, s20, s27
	s_add_i32 s33, s33, s36
	s_add_i32 s6, s6, s37
	s_cmpk_gt_i32 s20, 0x7ff
	s_cbranch_scc0 .LBB0_1601

; __device__ __forceinline__ void n1_phase(const Args& a, int layer, bool final_only, const int wv, const bool dry = false) {
;     ...
; #pragma unroll 1
;         for (int i = 0; i < 16; ++i) {
;             const int tok = tok0 + i;
;             f32x4 v[4];
;             if (layer == 0) ld_row16(a.x + (size_t)tok * DM, F.lane, v);
;             else {
; #pragma unroll
;                 for (int j = 0; j < 4; ++j) { const u32x2 w = *(const u32x2*)(XB + (size_t)tok * DM + 4 * F.lane + 256 * j); v[j] = (f32x4){bf_lo(w.x), bf_hi(w.x), bf_lo(w.y), bf_hi(w.y)}; } }
;             if (combine) {
;                 f32x4 ysum[4];
; #pragma unroll
;                 for (int j = 0; j < 4; ++j) ysum[j] = (f32x4){0.f, 0.f, 0.f, 0.f};
; #pragma unroll
;                 for (int k = 0; k < 4; ++k) { const int e = toke[tok * 4 + k], r = tokr[tok * 4 + k]; const size_t slot = (size_t)ps[e] + r;
;                     const unsigned char* yr = Y + slot * DM + 4 * F.lane;
; #pragma unroll
;                     for (int j = 0; j < 4; ++j) { const int w = *(const int*)(yr + 256 * j); const f32x2 lo = __builtin_amdgcn_cvt_pk_f32_fp8(w, false), hi = __builtin_amdgcn_cvt_pk_f32_fp8(w, true);
;                         ysum[j][0] += lo[0]; ysum[j][1] += lo[1]; ysum[j][2] += hi[0]; ysum[j][3] += hi[1]; } }
.LBB0_2706:
	v_lshl_add_u64 v[66:67], v[30:31], 0, s[10:11]
	s_add_i32 s14, s12, -3
	v_add_co_u32_e64 v68, s[2:3], s39, v66
	s_ashr_i32 s15, s14, 31
	s_nop 0
	v_addc_co_u32_e64 v69, s[2:3], 0, v67, s[2:3]
	s_lshl_b64 s[2:3], s[14:15], 2
	s_add_u32 s14, s21, s2
	s_addc_u32 s15, s22, s3
	v_add_co_u32_e32 v64, vcc, 0xaf200000, v66
	s_add_u32 s2, s23, s2
	s_nop 0
	v_addc_co_u32_e32 v65, vcc, 0, v67, vcc
	s_addc_u32 s3, s24, s3
	global_load_dwordx2 v[66:67], v[64:65], off
	global_load_dwordx2 v[80:81], v[64:65], off offset:512
	global_load_dwordx2 v[82:83], v[64:65], off offset:1024
	global_load_dwordx2 v[84:85], v[64:65], off offset:1536
	global_load_dword v87, v17, s[14:15]
	global_load_dword v86, v17, s[2:3]
	s_add_i32 s14, s12, -2
	s_ashr_i32 s15, s14, 31
	s_lshl_b64 s[2:3], s[14:15], 2
	s_add_u32 s14, s21, s2
	s_addc_u32 s15, s22, s3
	s_add_u32 s2, s23, s2
	s_addc_u32 s3, s24, s3
	global_load_dword v89, v17, s[14:15]
	global_load_dword v88, v17, s[2:3]
	s_add_i32 s14, s12, -1
	s_ashr_i32 s15, s14, 31
	s_lshl_b64 s[2:3], s[14:15], 2
	s_add_u32 s14, s21, s2
	s_addc_u32 s15, s22, s3
	s_add_u32 s2, s23, s2
	global_load_dword v91, v17, s[14:15]
	s_addc_u32 s3, s24, s3
	s_ashr_i32 s13, s12, 31
	global_load_dword v90, v17, s[2:3]
	s_lshl_b64 s[2:3], s[12:13], 2
	s_add_u32 s14, s21, s2
	s_addc_u32 s15, s22, s3
	global_load_dword v93, v17, s[14:15]
	s_add_u32 s2, s23, s2
	s_addc_u32 s3, s24, s3
	global_load_dword v92, v17, s[2:3]
	s_add_u32 s10, s10, 0x800
	s_addc_u32 s11, s11, 0
	s_add_i32 s12, s12, 4
	s_cmpk_eq_u32 s10, 0x8000
	s_waitcnt vmcnt(11)
	v_lshlrev_b32_e32 v94, 16, v66
	v_and_b32_e32 v95, 0xffff0000, v66
	v_lshlrev_b32_e32 v66, 16, v67
	v_and_b32_e32 v67, 0xffff0000, v67
	s_waitcnt vmcnt(7)
	v_lshlrev_b32_e32 v87, 2, v87
	v_add_u32_e32 v87, s37, v87
	ds_read_b32 v102, v87
	v_lshlrev_b32_e32 v96, 16, v80
	v_and_b32_e32 v97, 0xffff0000, v80
	v_lshlrev_b32_e32 v80, 16, v81
	v_and_b32_e32 v81, 0xffff0000, v81
	v_lshlrev_b32_e32 v98, 16, v82
	v_and_b32_e32 v99, 0xffff0000, v82
	s_waitcnt vmcnt(5)
	v_lshlrev_b32_e32 v89, 2, v89
	v_add_u32_e32 v89, s37, v89
	ds_read_b32 v104, v89
	v_ashrrev_i32_e32 v87, 31, v86
	s_waitcnt lgkmcnt(1)
	v_ashrrev_i32_e32 v103, 31, v102
	v_lshl_add_u64 v[86:87], v[102:103], 0, v[86:87]
	v_lshlrev_b64 v[86:87], 10, v[86:87]
	v_lshl_add_u64 v[86:87], v[18:19], 0, v[86:87]
	global_load_dword v102, v[86:87], off
	global_load_dword v103, v[86:87], off offset:256
	global_load_dword v106, v[86:87], off offset:512
	global_load_dword v108, v[86:87], off offset:768
	s_waitcnt vmcnt(7)
	v_lshlrev_b32_e32 v86, 2, v91
	v_add_u32_e32 v86, s37, v86
	v_ashrrev_i32_e32 v89, 31, v88
	ds_read_b32 v86, v86
	s_waitcnt lgkmcnt(1)
	v_ashrrev_i32_e32 v105, 31, v104
	v_lshl_add_u64 v[88:89], v[104:105], 0, v[88:89]
	v_lshlrev_b64 v[88:89], 10, v[88:89]
	s_waitcnt vmcnt(5)
	v_lshlrev_b32_e32 v87, 2, v93
	v_lshl_add_u64 v[88:89], v[18:19], 0, v[88:89]
	v_add_u32_e32 v87, s37, v87
	global_load_dword v112, v[88:89], off
	global_load_dword v116, v[88:89], off offset:256
	global_load_dword v120, v[88:89], off offset:512
	global_load_dword v124, v[88:89], off offset:768
	ds_read_b32 v88, v87
	v_ashrrev_i32_e32 v91, 31, v90
	s_waitcnt lgkmcnt(1)
	v_ashrrev_i32_e32 v87, 31, v86
	v_lshl_add_u64 v[86:87], v[86:87], 0, v[90:91]
	v_lshlrev_b64 v[86:87], 10, v[86:87]
	v_lshl_add_u64 v[86:87], v[18:19], 0, v[86:87]
	s_waitcnt vmcnt(8)
	v_ashrrev_i32_e32 v93, 31, v92
	global_load_dword v126, v[86:87], off
	global_load_dword v127, v[86:87], off offset:256
	global_load_dword v128, v[86:87], off offset:512
	global_load_dword v129, v[86:87], off offset:768
	s_waitcnt lgkmcnt(0)
	v_ashrrev_i32_e32 v89, 31, v88
	v_lshl_add_u64 v[86:87], v[88:89], 0, v[92:93]
	v_lshlrev_b64 v[86:87], 10, v[86:87]
	v_lshl_add_u64 v[86:87], v[18:19], 0, v[86:87]
	global_load_dword v130, v[86:87], off
	global_load_dword v131, v[86:87], off offset:256
	global_load_dword v132, v[86:87], off offset:512
	global_load_dword v133, v[86:87], off offset:768
	v_lshlrev_b32_e32 v100, 16, v84
	v_and_b32_e32 v101, 0xffff0000, v84
	v_lshlrev_b32_e32 v82, 16, v83
	v_and_b32_e32 v83, 0xffff0000, v83
	v_lshlrev_b32_e32 v84, 16, v85
	v_and_b32_e32 v85, 0xffff0000, v85
	s_waitcnt vmcnt(15)
	v_cvt_pk_f32_fp8_e32 v[86:87], v102
	v_cvt_pk_f32_fp8_sdwa v[88:89], v102 src0_sel:WORD_1
	s_waitcnt vmcnt(14)
	v_cvt_pk_f32_fp8_e32 v[90:91], v103
	v_cvt_pk_f32_fp8_sdwa v[92:93], v103 src0_sel:WORD_1
	s_waitcnt vmcnt(13)
	v_cvt_pk_f32_fp8_e32 v[102:103], v106
	v_cvt_pk_f32_fp8_sdwa v[104:105], v106 src0_sel:WORD_1
	s_waitcnt vmcnt(12)
	v_cvt_pk_f32_fp8_e32 v[106:107], v108
	v_cvt_pk_f32_fp8_sdwa v[108:109], v108 src0_sel:WORD_1
	v_pk_add_f32 v[88:89], v[88:89], 0 op_sel_hi:[1,0]
	v_pk_add_f32 v[86:87], v[86:87], 0 op_sel_hi:[1,0]
	v_pk_add_f32 v[90:91], v[90:91], 0 op_sel_hi:[1,0]
	s_waitcnt vmcnt(11)
	v_cvt_pk_f32_fp8_e32 v[110:111], v112
	v_cvt_pk_f32_fp8_sdwa v[112:113], v112 src0_sel:WORD_1
	s_waitcnt vmcnt(10)
	v_cvt_pk_f32_fp8_e32 v[114:115], v116
	v_cvt_pk_f32_fp8_sdwa v[116:117], v116 src0_sel:WORD_1
	s_waitcnt vmcnt(9)
	v_cvt_pk_f32_fp8_e32 v[118:119], v120
	s_waitcnt vmcnt(8)
	v_cvt_pk_f32_fp8_e32 v[122:123], v124
	v_cvt_pk_f32_fp8_sdwa v[120:121], v120 src0_sel:WORD_1
	v_cvt_pk_f32_fp8_sdwa v[124:125], v124 src0_sel:WORD_1
	v_pk_add_f32 v[92:93], v[92:93], 0 op_sel_hi:[1,0]
	v_pk_add_f32 v[102:103], v[102:103], 0 op_sel_hi:[1,0]
	v_pk_add_f32 v[106:107], v[106:107], 0 op_sel_hi:[1,0]
	v_pk_add_f32 v[86:87], v[86:87], v[110:111]
	v_pk_add_f32 v[88:89], v[88:89], v[112:113]
	v_pk_add_f32 v[90:91], v[90:91], v[114:115]
	s_waitcnt vmcnt(7)
	v_cvt_pk_f32_fp8_e32 v[110:111], v126
	v_cvt_pk_f32_fp8_sdwa v[112:113], v126 src0_sel:WORD_1
	s_waitcnt vmcnt(6)
; __device__ __forceinline__ unsigned cvt_pk_bf16(float lo, float hi) { unsigned r; asm volatile("v_cvt_pk_bf16_f32 %0, %1, %2" : "=v"(r) : "v"(lo), "v"(hi)); return r; }
; __device__ __forceinline__ float shx(float v, int m, int lane) { return __builtin_bit_cast(float, __builtin_amdgcn_ds_bpermute((lane ^ m) << 2, __builtin_bit_cast(int, v))); }
; __device__ __forceinline__ unsigned pk4_fp8c(float a, float b, float c, float d) { return pk4_fp8(__builtin_amdgcn_fmed3f(a, -448.f, 448.f), __builtin_amdgcn_fmed3f(b, -448.f, 448.f), __builtin_amdgcn_fmed3f(c, -448.f, 448.f), __builtin_amdgcn_fmed3f(d, -448.f, 448.f)); }
; __device__ __forceinline__ float wave_sum(float v, int lane) {
; #pragma unroll
;     for (int o = 1; o < 64; o <<= 1) v += shx(v, o, lane);
;     return v;
; __device__ __forceinline__ void n1_phase(const Args& a, int layer, bool final_only, const int wv, const bool dry = false) {
;     ...
; #pragma unroll
;                 for (int j = 0; j < 4; ++j) { v[j] = v[j] + g2s[j] * ysum[j];
;                     if (final_only) *(f32x4*)(a.out + (size_t)tok * DM + 4 * F.lane + 256 * j) = v[j];
;                     else { u32x2 o; o.x = cvt_pk_bf16(v[j][0], v[j][1]); o.y = cvt_pk_bf16(v[j][2], v[j][3]); *(u32x2*)((dry ? (bf16_t*)(ws + WS_ACT) : XB) + (size_t)tok * DM + 4 * F.lane + 256 * j) = o; } }
;             }
;             if (final_only) continue;
;             float ss = 0.f;
; #pragma unroll
;             for (int j = 0; j < 4; ++j) ss += v[j][0] * v[j][0] + v[j][1] * v[j][1] + v[j][2] * v[j][2] + v[j][3] * v[j][3];
;             const float inv = rsqrtf(wave_sum(ss, F.lane) * (1.f / DM) + EPS);
; #pragma unroll
;             for (int j = 0; j < 4; ++j) { const int c0 = 4 * F.lane + 256 * j;
;                 const f32x4 h = v[j] * inv * ma[j] + mb[j];
;                 if (layer & 1) *(unsigned*)((unsigned char*)HM + (size_t)tok * DM + c0) = pg8::pk4_fp8c(h[0] * FP8_HSC, h[1] * FP8_HSC, h[2] * FP8_HSC, h[3] * FP8_HSC);
;                 else { u32x2 o; o.x = cvt_pk_bf16(h[0], h[1]); o.y = cvt_pk_bf16(h[2], h[3]); *(u32x2*)(HM + (size_t)tok * DM + c0) = o; } }
	v_cvt_pk_f32_fp8_e32 v[114:115], v127
	v_pk_add_f32 v[92:93], v[92:93], v[116:117]
	v_pk_add_f32 v[102:103], v[102:103], v[118:119]
	v_pk_add_f32 v[106:107], v[106:107], v[122:123]
	v_cvt_pk_f32_fp8_sdwa v[116:117], v127 src0_sel:WORD_1
	s_waitcnt vmcnt(5)
	v_cvt_pk_f32_fp8_e32 v[118:119], v128
	s_waitcnt vmcnt(4)
	v_cvt_pk_f32_fp8_e32 v[122:123], v129
	v_pk_add_f32 v[104:105], v[104:105], 0 op_sel_hi:[1,0]
	v_pk_add_f32 v[108:109], v[108:109], 0 op_sel_hi:[1,0]
	v_pk_add_f32 v[104:105], v[104:105], v[120:121]
	v_pk_add_f32 v[108:109], v[108:109], v[124:125]
	v_cvt_pk_f32_fp8_sdwa v[120:121], v128 src0_sel:WORD_1
	v_cvt_pk_f32_fp8_sdwa v[124:125], v129 src0_sel:WORD_1
	v_pk_add_f32 v[88:89], v[88:89], v[112:113]
	v_pk_add_f32 v[86:87], v[86:87], v[110:111]
	v_pk_add_f32 v[90:91], v[90:91], v[114:115]
	s_waitcnt vmcnt(3)
	v_cvt_pk_f32_fp8_e32 v[110:111], v130
	v_cvt_pk_f32_fp8_sdwa v[112:113], v130 src0_sel:WORD_1
	s_waitcnt vmcnt(2)
	v_cvt_pk_f32_fp8_e32 v[114:115], v131
	v_pk_add_f32 v[92:93], v[92:93], v[116:117]
	v_pk_add_f32 v[102:103], v[102:103], v[118:119]
	v_pk_add_f32 v[106:107], v[106:107], v[122:123]
	v_cvt_pk_f32_fp8_sdwa v[116:117], v131 src0_sel:WORD_1
	s_waitcnt vmcnt(1)
	v_cvt_pk_f32_fp8_e32 v[118:119], v132
	s_waitcnt vmcnt(0)
	v_cvt_pk_f32_fp8_e32 v[122:123], v133
	v_pk_add_f32 v[104:105], v[104:105], v[120:121]
	v_pk_add_f32 v[108:109], v[108:109], v[124:125]
	v_cvt_pk_f32_fp8_sdwa v[120:121], v132 src0_sel:WORD_1
	v_cvt_pk_f32_fp8_sdwa v[124:125], v133 src0_sel:WORD_1
	v_pk_add_f32 v[86:87], v[86:87], v[110:111]
	v_pk_add_f32 v[88:89], v[88:89], v[112:113]
	v_pk_add_f32 v[90:91], v[90:91], v[114:115]
	v_pk_add_f32 v[92:93], v[92:93], v[116:117]
	v_pk_add_f32 v[102:103], v[102:103], v[118:119]
	v_pk_add_f32 v[106:107], v[106:107], v[122:123]
	v_pk_fma_f32 v[66:67], v[40:41], v[88:89], v[66:67]
	v_pk_fma_f32 v[86:87], v[42:43], v[86:87], v[94:95]
	v_pk_fma_f32 v[88:89], v[34:35], v[90:91], v[96:97]
	v_pk_fma_f32 v[80:81], v[32:33], v[92:93], v[80:81]
	v_pk_fma_f32 v[90:91], v[38:39], v[102:103], v[98:99]
	v_pk_fma_f32 v[92:93], v[46:47], v[106:107], v[100:101]
	v_mov_b32_e32 v98, v87
	v_mov_b32_e32 v99, v89
	v_pk_add_f32 v[104:105], v[104:105], v[120:121]
	v_pk_add_f32 v[108:109], v[108:109], v[124:125]
	v_cvt_pk_bf16_f32 v94, v86, v87
	v_cvt_pk_bf16_f32 v95, v66, v67
	v_mov_b32_e32 v96, v86
	v_mov_b32_e32 v97, v88
	v_mov_b32_e32 v106, v91
	v_mov_b32_e32 v107, v93
	v_pk_mul_f32 v[98:99], v[98:99], v[98:99]
	v_pk_fma_f32 v[82:83], v[36:37], v[104:105], v[82:83]
	v_pk_fma_f32 v[84:85], v[44:45], v[108:109], v[84:85]
	v_mov_b32_e32 v100, v66
	v_mov_b32_e32 v101, v80
	v_mov_b32_e32 v104, v90
	v_mov_b32_e32 v105, v92
	global_store_dwordx2 v[64:65], v[94:95], off
	v_cvt_pk_bf16_f32 v94, v88, v89
	v_cvt_pk_bf16_f32 v95, v80, v81
	v_pk_mul_f32 v[106:107], v[106:107], v[106:107]
	v_pk_fma_f32 v[96:97], v[96:97], v[96:97], v[98:99]
	v_mov_b32_e32 v102, v67
	v_mov_b32_e32 v103, v81
	v_mov_b32_e32 v108, v82
	v_mov_b32_e32 v109, v84
	global_store_dwordx2 v[64:65], v[94:95], off offset:512
	v_cvt_pk_bf16_f32 v94, v90, v91
	v_cvt_pk_bf16_f32 v95, v82, v83
	v_pk_fma_f32 v[98:99], v[104:105], v[104:105], v[106:107]
	v_pk_fma_f32 v[96:97], v[100:101], v[100:101], v[96:97]
	v_mov_b32_e32 v110, v83
	v_mov_b32_e32 v111, v85
	global_store_dwordx2 v[64:65], v[94:95], off offset:1024
	v_cvt_pk_bf16_f32 v94, v92, v93
	v_cvt_pk_bf16_f32 v95, v84, v85
	v_pk_fma_f32 v[98:99], v[108:109], v[108:109], v[98:99]
	global_store_dwordx2 v[64:65], v[94:95], off offset:1536
	v_pk_fma_f32 v[64:65], v[102:103], v[102:103], v[96:97]
	v_pk_fma_f32 v[94:95], v[110:111], v[110:111], v[98:99]
	v_add_f32_e32 v64, v64, v65
	v_add_f32_e32 v64, v64, v94
	v_add_f32_e32 v64, v64, v95
	s_waitcnt lgkmcnt(0)
	s_nop 1
	v_add_f32_dpp v64, v64, v64 quad_perm:[1,0,3,2] row_mask:0xf bank_mask:0xf
	s_nop 1
	v_add_f32_dpp v64, v64, v64 quad_perm:[2,3,0,1] row_mask:0xf bank_mask:0xf
	s_nop 1
	v_add_f32_dpp v64, v64, v64 row_half_mirror row_mask:0xf bank_mask:0xf
	s_nop 1
	v_add_f32_dpp v64, v64, v64 row_mirror row_mask:0xf bank_mask:0xf
	v_mov_b32_e32 v65, v64
	s_nop 1
	v_permlane16_swap_b32_e32 v64, v65
	v_add_f32_e32 v64, v64, v65
	v_mov_b32_e32 v65, v64
	s_nop 1
	v_permlane32_swap_b32_e32 v64, v65
	v_add_f32_e32 v64, v64, v65
	v_fmamk_f32 v64, v64, 0x3a800000, v79
	v_mul_f32_e32 v65, 0x4b800000, v64
	v_cmp_gt_f32_e32 vcc, s38, v64
	s_nop 1
	v_cndmask_b32_e32 v64, v64, v65, vcc
	v_rsq_f32_e32 v64, v64
	s_nop 0
	v_mul_f32_e32 v65, 0x45800000, v64
	v_cndmask_b32_e32 v64, v64, v65, vcc
	v_pk_mul_f32 v[86:87], v[86:87], v[64:65] op_sel_hi:[1,0]
	v_pk_mul_f32 v[66:67], v[66:67], v[64:65] op_sel_hi:[1,0]
	v_pk_mul_f32 v[88:89], v[88:89], v[64:65] op_sel_hi:[1,0]
	v_pk_mul_f32 v[80:81], v[80:81], v[64:65] op_sel_hi:[1,0]
	v_pk_mul_f32 v[90:91], v[90:91], v[64:65] op_sel_hi:[1,0]
	v_pk_mul_f32 v[82:83], v[82:83], v[64:65] op_sel_hi:[1,0]
	v_pk_mul_f32 v[92:93], v[92:93], v[64:65] op_sel_hi:[1,0]
	v_pk_mul_f32 v[64:65], v[84:85], v[64:65] op_sel_hi:[1,0]
	v_pk_fma_f32 v[66:67], v[48:49], v[66:67], v[2:3]
	v_pk_fma_f32 v[84:85], v[50:51], v[86:87], v[0:1]
	v_pk_fma_f32 v[80:81], v[52:53], v[80:81], v[6:7]
	v_pk_fma_f32 v[86:87], v[54:55], v[88:89], v[4:5]
	v_cvt_pk_bf16_f32 v84, v84, v85
	v_cvt_pk_bf16_f32 v85, v66, v67
	global_store_dwordx2 v[68:69], v[84:85], off
	v_cvt_pk_bf16_f32 v66, v86, v87
	v_cvt_pk_bf16_f32 v67, v80, v81
	v_pk_fma_f32 v[82:83], v[56:57], v[82:83], v[10:11]
	v_pk_fma_f32 v[88:89], v[58:59], v[90:91], v[8:9]
	global_store_dwordx2 v[68:69], v[66:67], off offset:512
	v_cvt_pk_bf16_f32 v66, v88, v89
	v_cvt_pk_bf16_f32 v67, v82, v83
	v_pk_fma_f32 v[64:65], v[60:61], v[64:65], v[14:15]
	v_pk_fma_f32 v[90:91], v[62:63], v[92:93], v[12:13]
	global_store_dwordx2 v[68:69], v[66:67], off offset:1024
	v_cvt_pk_bf16_f32 v66, v90, v91
	v_cvt_pk_bf16_f32 v67, v64, v65
	global_store_dwordx2 v[68:69], v[66:67], off offset:1536
	s_cbranch_scc0 .LBB0_2706
	s_add_i32 s9, s9, s25
	s_add_i32 s26, s26, s27
	s_add_i32 s4, s4, s33
	s_cmpk_gt_i32 s9, 0x7ff
	s_cbranch_scc0 .LBB0_2705
